# gemm_in tail round: each of the 112 leftover 256x256 tiles is shared by two workgroups (c and c+112), each running a trimmed copy of the 8-phase loop that computes one 128-row half (half the MFMA bloc
# baseline (speedup 1.0000x reference)
.LBB0_258:
	s_or_b64 exec, exec, s[0:1]
	s_abs_i32 s7, s79
	s_waitcnt lgkmcnt(0)
	v_cvt_f32_u32_e32 v2, s7
	s_sub_i32 s5, 0, s7
	s_mov_b64 s[0:1], s[72:73]
	s_mov_b32 s4, s2
	v_rcp_iflag_f32_e32 v2, v2
	s_barrier
	v_mul_f32_e32 v2, 0x4f7ffffe, v2
	v_cvt_u32_f32_e32 v2, v2
	s_nop 0
	v_readfirstlane_b32 s6, v2
	s_mul_i32 s5, s5, s6
	s_mul_hi_u32 s5, s6, s5
	s_add_i32 s5, s6, s5
	v_writelane_b32 v255, s5, 27
	s_mul_hi_u32 s5, s5, 0x770
	s_mul_i32 s5, s5, s7
	s_sub_i32 s5, 0x770, s5
	s_sub_i32 s6, s5, s7
	s_cmp_ge_u32 s5, s7
	s_cselect_b32 s5, s6, s5
	s_sub_i32 s6, s5, s7
	s_cmp_ge_u32 s5, s7
	s_cselect_b32 s5, s6, s5
	s_cmp_eq_u32 s5, 0
	v_writelane_b32 v255, s7, 28
	s_cselect_b64 s[6:7], -1, 0
	s_cmp_lt_i32 s4, s5
	s_cselect_b64 s[8:9], -1, 0
	s_or_b64 s[6:7], s[6:7], s[8:9]
	s_and_b64 vcc, exec, s[6:7]
	s_branch .LBB0_261
	s_sub_i32 s4, s4, s5
	s_and_b32 s4, s4, 3
	s_mul_i32 s8, s4, 0x20d0
	s_memrealtime s[4:5]
	s_memrealtime s[6:7]
	s_addk_i32 s8, 0x20d0
	s_waitcnt lgkmcnt(0)
	s_and_b32 s5, s8, 0xfff0
	s_mul_i32 s5, s5, 0xcccd
	s_lshr_b32 s5, s5, 20
	s_sub_i32 s6, s6, s4
	s_cmp_le_u32 s5, s6
	s_cbranch_scc1 .LBB0_261

.LBB0_264:
	v_lshrrev_b32_e32 v14, 1, v11
	v_and_b32_e32 v14, 24, v14
	v_and_b32_e32 v13, 15, v11
	v_lshlrev_b32_e32 v15, 1, v14
	v_lshlrev_b32_e32 v11, 2, v11
	s_sext_i32_i8 s40, s0
	v_lshl_or_b32 v147, s1, 6, v13
	v_lshl_or_b32 v13, v13, 6, v15
	s_lshl_b32 s0, s1, 13
	v_and_b32_e32 v11, 32, v11
	v_bitop3_b32 v15, v13, s0, v11 bitop3:0xde
	s_lshl_b32 s0, s4, 5
	s_and_b32 s4, s0, 0x60
	s_add_i32 m0, s28, 0x18000
	v_lshl_add_u64 v[8:9], v[8:9], 0, s[96:97]
	s_lshl_b32 s0, s4, 7
	s_waitcnt vmcnt(4)
	s_barrier
	global_load_lds_dwordx4 v[8:9], off
	v_lshl_add_u64 v[6:7], v[6:7], 0, s[96:97]
	s_add_i32 m0, s28, 0x1a000
	s_add_i32 s34, s28, 0x8000
	s_add_i32 s35, s28, 0xa000
	v_bitop3_b32 v148, v13, s0, v11 bitop3:0xde
	global_load_lds_dwordx4 v[6:7], off
	v_lshl_add_u64 v[4:5], v[4:5], 0, s[96:97]
	s_mov_b32 m0, s34
	s_add_u32 s0, s16, 0x40080
	global_load_lds_dwordx4 v[4:5], off
	v_lshl_add_u64 v[2:3], v[2:3], 0, s[96:97]
	s_mov_b32 m0, s35
	s_addc_u32 s1, s17, 0
	global_load_lds_dwordx4 v[2:3], off
	s_add_i32 m0, s28, 0x1c000
	v_lshl_add_u64 v[2:3], s[0:1], 0, v[132:133]
	global_load_lds_dwordx4 v[2:3], off
	v_lshl_add_u64 v[2:3], s[0:1], 0, v[130:131]
	s_add_i32 m0, s28, 0x1e000
	s_ashr_i32 s36, s79, 31
	global_load_lds_dwordx4 v[2:3], off
	s_waitcnt vmcnt(6)
	s_add_u32 s0, s8, 0x80
	v_add_u32_e32 v149, v10, v12
	v_or_b32_e32 v150, s4, v14
	s_addc_u32 s1, s9, 0
	s_mov_b32 s37, 0
	v_add_u32_e32 v151, 0, v15
	s_mov_b32 s101, 2
	s_barrier
.LBB0_265:
	s_mov_b32 s100, s101
	s_add_i32 s37, s37, 1
	s_mul_i32 s4, s37, s36
	s_mul_hi_u32 s5, s37, s79
	s_add_i32 s5, s5, s4
	s_mul_i32 s4, s37, s79
	s_add_u32 s14, s4, s22
	s_addc_u32 s15, s5, s27
	s_mov_b32 s101, 2
	s_cmp_lg_u32 s37, 7
	s_cbranch_scc1 .Lgi_mode_done
	s_mov_b32 s101, 0
	s_cmpk_lt_u32 s22, 0x70
	s_cbranch_scc1 .Lgi_mode_done
	s_mov_b32 s101, 2
	s_cmpk_ge_u32 s22, 0xe0
	s_cbranch_scc1 .Lgi_mode_done
	s_mov_b32 s101, 1
	s_sub_u32 s14, s14, 0x70
	s_subb_u32 s15, s15, 0
.Lgi_mode_done:
	v_mov_b64_e32 v[2:3], 0x770
	v_cmp_lt_i64_e64 s[6:7], s[14:15], v[2:3]
	v_mov_b64_e32 v[2:3], 0x76f
	v_cmp_gt_i64_e64 s[4:5], s[14:15], v[2:3]
	s_and_b64 vcc, exec, s[4:5]
	s_cbranch_vccnz .LBB0_267
	s_ashr_i32 s12, s14, 31
	s_lshr_b32 s12, s12, 29
	s_add_i32 s12, s14, s12
	s_ashr_i32 s13, s12, 3
	s_and_b32 s12, s12, -8
	s_sub_i32 s12, s14, s12
	s_cmp_lt_i32 s12, 0
	s_movk_i32 s14, 0xef
	s_cselect_b32 s14, s14, 0xee
	s_mul_i32 s12, s14, s12
	s_add_i32 s12, s12, s13
	s_mul_hi_i32 s13, s12, 0x92492493
	s_add_i32 s13, s13, s12
	s_lshr_b32 s14, s13, 31
	s_ashr_i32 s13, s13, 6
	s_add_i32 s13, s13, s14
	s_lshl_b32 s14, s13, 3
	s_sub_i32 s15, 0x88, s14
	s_min_i32 s15, s15, 8
	s_abs_i32 s18, s15
	v_cvt_f32_u32_e32 v2, s18
	s_sub_i32 s20, 0, s18
	s_mulk_i32 s13, 0x70
	s_sub_i32 s13, s12, s13
	v_rcp_iflag_f32_e32 v2, v2
	s_abs_i32 s12, s13
	s_xor_b32 s19, s13, s15
	s_ashr_i32 s19, s19, 31
	v_mul_f32_e32 v2, 0x4f7ffffe, v2
	v_cvt_u32_f32_e32 v2, v2
	s_nop 0
	v_readfirstlane_b32 s21, v2
	s_mul_i32 s20, s20, s21
	s_mul_hi_u32 s20, s21, s20
	s_add_i32 s21, s21, s20
	s_mul_hi_u32 s20, s12, s21
	s_mul_i32 s21, s20, s18
	s_sub_i32 s12, s12, s21
	s_add_i32 s33, s20, 1
	s_sub_i32 s21, s12, s18
	s_cmp_ge_u32 s12, s18
	s_cselect_b32 s20, s33, s20
	s_cselect_b32 s12, s21, s12
	s_add_i32 s21, s20, 1
	s_cmp_ge_u32 s12, s18
	s_cselect_b32 s12, s21, s20
	s_xor_b32 s12, s12, s19
	s_sub_i32 s12, s12, s19
	s_mul_i32 s15, s12, s15
	s_sub_i32 s13, s13, s15
	s_add_i32 s38, s13, s14
.LBB0_267:
	s_ashr_i32 s13, s12, 31
	s_lshl_b64 s[14:15], s[12:13], 19
	s_add_u32 s14, s24, s14
	s_addc_u32 s15, s25, s15
	s_lshl_b32 s13, s38, 18
	v_add_lshl_u32 v152, s13, v146, 1
	v_add_lshl_u32 v153, s13, v149, 1
	s_bitset1_b32 s13, 17
	s_and_b64 s[18:19], s[6:7], exec
	v_add_lshl_u32 v154, s13, v146, 1
	v_add_lshl_u32 v155, s13, v149, 1
	s_cselect_b32 s13, s15, s17
	s_cselect_b32 s41, s14, s16
	v_mov_b32_e32 v139, v227
	v_mov_b32_e32 v141, v227
	s_add_u32 s42, s16, 0x100
	v_mov_b32_e32 v2, 0
	v_lshl_add_u64 v[142:143], s[0:1], 0, v[140:141]
	v_lshl_add_u64 v[144:145], s[0:1], 0, v[138:139]
	s_addc_u32 s43, s17, 0
	s_mov_b32 s44, -2
	s_mov_b64 s[16:17], 0
	v_mov_b32_e32 v3, v2
	v_mov_b32_e32 v4, v2
	v_mov_b32_e32 v5, v2
	v_mov_b32_e32 v6, v2
	v_mov_b32_e32 v7, v2
	v_mov_b32_e32 v8, v2
	v_mov_b32_e32 v9, v2
	v_mov_b32_e32 v10, v2
	v_mov_b32_e32 v11, v2
	v_mov_b32_e32 v12, v2
	v_mov_b32_e32 v13, v2
	v_mov_b32_e32 v14, v2
	v_mov_b32_e32 v15, v2
	v_mov_b32_e32 v16, v2
	v_mov_b32_e32 v17, v2
	v_mov_b32_e32 v18, v2
	v_mov_b32_e32 v19, v2
	v_mov_b32_e32 v20, v2
	v_mov_b32_e32 v21, v2
	v_mov_b32_e32 v22, v2
	v_mov_b32_e32 v23, v2
	v_mov_b32_e32 v24, v2
	v_mov_b32_e32 v25, v2
	v_mov_b32_e32 v34, v2
	v_mov_b32_e32 v35, v2
	v_mov_b32_e32 v36, v2
	v_mov_b32_e32 v37, v2
	v_mov_b32_e32 v46, v2
	v_mov_b32_e32 v47, v2
	v_mov_b32_e32 v48, v2
	v_mov_b32_e32 v49, v2
	v_mov_b32_e32 v58, v2
	v_mov_b32_e32 v59, v2
	v_mov_b32_e32 v60, v2
	v_mov_b32_e32 v61, v2
	v_mov_b32_e32 v62, v2
	v_mov_b32_e32 v63, v2
	v_mov_b32_e32 v64, v2
	v_mov_b32_e32 v65, v2
	v_mov_b32_e32 v74, v2
	v_mov_b32_e32 v75, v2
	v_mov_b32_e32 v76, v2
	v_mov_b32_e32 v77, v2
	v_mov_b32_e32 v82, v2
	v_mov_b32_e32 v83, v2
	v_mov_b32_e32 v84, v2
	v_mov_b32_e32 v85, v2
	v_mov_b32_e32 v90, v2
	v_mov_b32_e32 v91, v2
	v_mov_b32_e32 v92, v2
	v_mov_b32_e32 v93, v2
	v_mov_b32_e32 v98, v2
	v_mov_b32_e32 v99, v2
	v_mov_b32_e32 v100, v2
	v_mov_b32_e32 v101, v2
	v_mov_b32_e32 v106, v2
	v_mov_b32_e32 v107, v2
	v_mov_b32_e32 v108, v2
	v_mov_b32_e32 v109, v2
	v_mov_b32_e32 v114, v2
	v_mov_b32_e32 v115, v2
	v_mov_b32_e32 v116, v2
	v_mov_b32_e32 v117, v2
	v_mov_b32_e32 v78, v2
	v_mov_b32_e32 v79, v2
	v_mov_b32_e32 v80, v2
	v_mov_b32_e32 v81, v2
	v_mov_b32_e32 v86, v2
	v_mov_b32_e32 v87, v2
	v_mov_b32_e32 v88, v2
	v_mov_b32_e32 v89, v2
	v_mov_b32_e32 v94, v2
	v_mov_b32_e32 v95, v2
	v_mov_b32_e32 v96, v2
	v_mov_b32_e32 v97, v2
	v_mov_b32_e32 v102, v2
	v_mov_b32_e32 v103, v2
	v_mov_b32_e32 v104, v2
	v_mov_b32_e32 v105, v2
	v_mov_b32_e32 v110, v2
	v_mov_b32_e32 v111, v2
	v_mov_b32_e32 v112, v2
	v_mov_b32_e32 v113, v2
	v_mov_b32_e32 v118, v2
	v_mov_b32_e32 v119, v2
	v_mov_b32_e32 v120, v2
	v_mov_b32_e32 v121, v2
	v_mov_b32_e32 v122, v2
	v_mov_b32_e32 v123, v2
	v_mov_b32_e32 v124, v2
	v_mov_b32_e32 v125, v2
	v_mov_b32_e32 v126, v2
	v_mov_b32_e32 v127, v2
	v_mov_b32_e32 v128, v2
	v_mov_b32_e32 v129, v2
	v_mov_b32_e32 v70, v2
	v_mov_b32_e32 v71, v2
	v_mov_b32_e32 v72, v2
	v_mov_b32_e32 v73, v2
	v_mov_b32_e32 v66, v2
	v_mov_b32_e32 v67, v2
	v_mov_b32_e32 v68, v2
	v_mov_b32_e32 v69, v2
	v_mov_b32_e32 v54, v2
	v_mov_b32_e32 v55, v2
	v_mov_b32_e32 v56, v2
	v_mov_b32_e32 v57, v2
	v_mov_b32_e32 v50, v2
	v_mov_b32_e32 v51, v2
	v_mov_b32_e32 v52, v2
	v_mov_b32_e32 v53, v2
	v_mov_b32_e32 v42, v2
	v_mov_b32_e32 v43, v2
	v_mov_b32_e32 v44, v2
	v_mov_b32_e32 v45, v2
	v_mov_b32_e32 v38, v2
	v_mov_b32_e32 v39, v2
	v_mov_b32_e32 v40, v2
	v_mov_b32_e32 v41, v2
	v_mov_b32_e32 v30, v2
	v_mov_b32_e32 v31, v2
	v_mov_b32_e32 v32, v2
	v_mov_b32_e32 v33, v2
	v_mov_b32_e32 v26, v2
	v_mov_b32_e32 v27, v2
	v_mov_b32_e32 v28, v2
	v_mov_b32_e32 v29, v2
	s_cmp_eq_u32 s100, 2
	s_cbranch_scc0 .Lgi_half
.LBB0_268:
	s_add_u32 s18, s8, s16
	s_addc_u32 s19, s9, s17
	s_add_u32 s20, s18, 0x100
	s_addc_u32 s21, s19, 0
	s_add_u32 s33, s42, s16
	s_addc_u32 s45, s43, s17
	s_cmpk_eq_i32 s16, 0x700
	s_cselect_b64 s[46:47], -1, 0
	s_and_b64 s[18:19], s[46:47], exec
	s_cselect_b32 s21, s9, s21
	s_cselect_b32 s20, s8, s20
	s_cselect_b32 s19, s13, s45
	s_cselect_b32 s18, s41, s33
	s_add_i32 s33, 0, 0x10000
	v_add_u32_e32 v135, s33, v148
	ds_read_b128 v[156:159], v135
	ds_read_b128 v[160:163], v135 offset:1024
	ds_read_b128 v[172:175], v135 offset:2048
	ds_read_b128 v[176:179], v135 offset:3072
	s_and_b64 vcc, s[6:7], s[46:47]
	v_cndmask_b32_e32 v226, v134, v152, vcc
	v_cndmask_b32_e32 v164, v136, v153, vcc
	v_cndmask_b32_e32 v135, v138, v154, vcc
	v_cndmask_b32_e32 v137, v140, v155, vcc
	v_lshl_add_u64 v[212:213], v[144:145], 0, s[16:17]
	s_add_i32 m0, s28, 0xc000
	ds_read_b128 v[180:183], v151
	ds_read_b128 v[184:187], v151 offset:1024
	ds_read_b128 v[188:191], v151 offset:2048
	ds_read_b128 v[192:195], v151 offset:3072
	ds_read_b128 v[196:199], v151 offset:4096
	ds_read_b128 v[200:203], v151 offset:5120
	ds_read_b128 v[204:207], v151 offset:6144
	ds_read_b128 v[208:211], v151 offset:7168
	global_load_lds_dwordx4 v[212:213], off
	v_lshl_add_u64 v[212:213], v[142:143], 0, s[16:17]
	s_add_i32 m0, s28, 0xe000
	s_nop 0
	global_load_lds_dwordx4 v[212:213], off
	s_waitcnt lgkmcnt(8)
	s_barrier
	s_waitcnt lgkmcnt(0)
	s_setprio 1
	s_waitcnt lgkmcnt(0)
	v_mfma_f32_16x16x32_bf16 v[126:129], v[156:159], v[180:183], v[126:129]
	v_mfma_f32_16x16x32_bf16 v[122:125], v[172:175], v[180:183], v[122:125]
	v_mfma_f32_16x16x32_bf16 v[118:121], v[156:159], v[188:191], v[118:121]
	v_mfma_f32_16x16x32_bf16 v[110:113], v[172:175], v[188:191], v[110:113]
	v_mfma_f32_16x16x32_bf16 v[102:105], v[156:159], v[196:199], v[102:105]
	v_mfma_f32_16x16x32_bf16 v[94:97], v[172:175], v[196:199], v[94:97]
	v_mfma_f32_16x16x32_bf16 v[86:89], v[156:159], v[204:207], v[86:89]
	v_mfma_f32_16x16x32_bf16 v[78:81], v[172:175], v[204:207], v[78:81]
	v_mfma_f32_16x16x32_bf16 v[126:129], v[160:163], v[184:187], v[126:129]
	v_mfma_f32_16x16x32_bf16 v[122:125], v[176:179], v[184:187], v[122:125]
	v_mfma_f32_16x16x32_bf16 v[118:121], v[160:163], v[192:195], v[118:121]
	v_mfma_f32_16x16x32_bf16 v[110:113], v[176:179], v[192:195], v[110:113]
	v_mfma_f32_16x16x32_bf16 v[102:105], v[160:163], v[200:203], v[102:105]
	v_mfma_f32_16x16x32_bf16 v[94:97], v[176:179], v[200:203], v[94:97]
	v_mfma_f32_16x16x32_bf16 v[86:89], v[160:163], v[208:211], v[86:89]
	v_mfma_f32_16x16x32_bf16 v[78:81], v[176:179], v[208:211], v[78:81]
	s_setprio 0
	s_barrier
	s_add_i32 s45, 0, 0x14000
	s_add_i32 s33, s33, s26
	v_add_u32_e32 v139, s45, v148
	v_lshl_add_u64 v[242:243], s[18:19], 0, v[132:133]
	s_mov_b32 m0, s33
	ds_read_b128 v[212:215], v139
	ds_read_b128 v[230:233], v139 offset:1024
	ds_read_b128 v[234:237], v139 offset:2048
	ds_read_b128 v[238:241], v139 offset:3072
	global_load_lds_dwordx4 v[242:243], off
	v_lshl_add_u64 v[244:245], s[18:19], 0, v[130:131]
	s_add_i32 m0, s33, 0x2000
	s_nop 0
	global_load_lds_dwordx4 v[244:245], off
	s_barrier
	s_waitcnt lgkmcnt(0)
	s_setprio 1
	s_waitcnt lgkmcnt(0)
	v_mfma_f32_16x16x32_bf16 v[114:117], v[212:215], v[180:183], v[114:117]
	v_mfma_f32_16x16x32_bf16 v[106:109], v[234:237], v[180:183], v[106:109]
	v_mfma_f32_16x16x32_bf16 v[98:101], v[212:215], v[188:191], v[98:101]
	v_mfma_f32_16x16x32_bf16 v[90:93], v[234:237], v[188:191], v[90:93]
	v_mfma_f32_16x16x32_bf16 v[82:85], v[212:215], v[196:199], v[82:85]
	v_mfma_f32_16x16x32_bf16 v[74:77], v[234:237], v[196:199], v[74:77]
	v_mfma_f32_16x16x32_bf16 v[62:65], v[212:215], v[204:207], v[62:65]
	v_mfma_f32_16x16x32_bf16 v[58:61], v[234:237], v[204:207], v[58:61]
	v_mfma_f32_16x16x32_bf16 v[114:117], v[230:233], v[184:187], v[114:117]
	v_mfma_f32_16x16x32_bf16 v[106:109], v[238:241], v[184:187], v[106:109]
	v_mfma_f32_16x16x32_bf16 v[98:101], v[230:233], v[192:195], v[98:101]
	v_mfma_f32_16x16x32_bf16 v[90:93], v[238:241], v[192:195], v[90:93]
	v_mfma_f32_16x16x32_bf16 v[82:85], v[230:233], v[200:203], v[82:85]
	v_mfma_f32_16x16x32_bf16 v[74:77], v[238:241], v[200:203], v[74:77]
	v_mfma_f32_16x16x32_bf16 v[62:65], v[230:233], v[208:211], v[62:65]
	v_mfma_f32_16x16x32_bf16 v[58:61], v[238:241], v[208:211], v[58:61]
	s_setprio 0
	s_mov_b32 m0, s28
	s_barrier
	ds_read_b128 v[180:183], v151 offset:16384
	ds_read_b128 v[184:187], v151 offset:17408
	ds_read_b128 v[188:191], v151 offset:18432
	ds_read_b128 v[192:195], v151 offset:19456
	ds_read_b128 v[196:199], v151 offset:20480
	ds_read_b128 v[200:203], v151 offset:21504
	ds_read_b128 v[204:207], v151 offset:22528
	ds_read_b128 v[208:211], v151 offset:23552
	global_load_lds_dwordx4 v226, s[20:21]
	s_mov_b32 m0, s29
	v_mov_b32_e32 v165, v227
	global_load_lds_dwordx4 v164, s[20:21]
	s_barrier
	s_waitcnt lgkmcnt(0)
	v_lshl_add_u64 v[246:247], s[20:21], 0, v[226:227]
	v_lshl_add_u64 v[164:165], s[20:21], 0, v[164:165]
	s_setprio 1
	s_waitcnt lgkmcnt(0)
	v_mfma_f32_16x16x32_bf16 v[46:49], v[156:159], v[180:183], v[46:49]
	v_mfma_f32_16x16x32_bf16 v[34:37], v[172:175], v[180:183], v[34:37]
	v_mfma_f32_16x16x32_bf16 v[22:25], v[156:159], v[188:191], v[22:25]
	v_mfma_f32_16x16x32_bf16 v[18:21], v[172:175], v[188:191], v[18:21]
	v_mfma_f32_16x16x32_bf16 v[14:17], v[156:159], v[196:199], v[14:17]
	v_mfma_f32_16x16x32_bf16 v[10:13], v[172:175], v[196:199], v[10:13]
	v_mfma_f32_16x16x32_bf16 v[6:9], v[156:159], v[204:207], v[6:9]
	v_mfma_f32_16x16x32_bf16 v[2:5], v[172:175], v[204:207], v[2:5]
	v_mfma_f32_16x16x32_bf16 v[46:49], v[160:163], v[184:187], v[46:49]
	v_mfma_f32_16x16x32_bf16 v[34:37], v[176:179], v[184:187], v[34:37]
	v_mfma_f32_16x16x32_bf16 v[22:25], v[160:163], v[192:195], v[22:25]
	v_mfma_f32_16x16x32_bf16 v[18:21], v[176:179], v[192:195], v[18:21]
	v_mfma_f32_16x16x32_bf16 v[14:17], v[160:163], v[200:203], v[14:17]
	v_mfma_f32_16x16x32_bf16 v[10:13], v[176:179], v[200:203], v[10:13]
	v_mfma_f32_16x16x32_bf16 v[6:9], v[160:163], v[208:211], v[6:9]
	v_mfma_f32_16x16x32_bf16 v[2:5], v[176:179], v[208:211], v[2:5]
	s_setprio 0
	s_barrier
	s_add_u32 s46, s18, 0x40000
	s_addc_u32 s47, s19, 0
	s_add_i32 s33, s45, s26
	v_lshl_add_u64 v[156:157], s[46:47], 0, v[132:133]
	s_mov_b32 m0, s33
	s_nop 0
	global_load_lds_dwordx4 v[156:157], off
	v_lshl_add_u64 v[156:157], s[46:47], 0, v[130:131]
	s_add_i32 m0, s33, 0x2000
	s_nop 0
	global_load_lds_dwordx4 v[156:157], off
	s_waitcnt vmcnt(6)
	s_barrier
	s_setprio 1
	v_mfma_f32_16x16x32_bf16 v[70:73], v[212:215], v[180:183], v[70:73]
	v_mfma_f32_16x16x32_bf16 v[66:69], v[234:237], v[180:183], v[66:69]
	v_mfma_f32_16x16x32_bf16 v[54:57], v[212:215], v[188:191], v[54:57]
	v_mfma_f32_16x16x32_bf16 v[50:53], v[234:237], v[188:191], v[50:53]
	v_mfma_f32_16x16x32_bf16 v[42:45], v[212:215], v[196:199], v[42:45]
	v_mfma_f32_16x16x32_bf16 v[38:41], v[234:237], v[196:199], v[38:41]
	v_mfma_f32_16x16x32_bf16 v[30:33], v[212:215], v[204:207], v[30:33]
	v_mfma_f32_16x16x32_bf16 v[26:29], v[234:237], v[204:207], v[26:29]
	v_mfma_f32_16x16x32_bf16 v[70:73], v[230:233], v[184:187], v[70:73]
	v_mfma_f32_16x16x32_bf16 v[66:69], v[238:241], v[184:187], v[66:69]
	v_mfma_f32_16x16x32_bf16 v[54:57], v[230:233], v[192:195], v[54:57]
	v_mfma_f32_16x16x32_bf16 v[50:53], v[238:241], v[192:195], v[50:53]
	v_mfma_f32_16x16x32_bf16 v[42:45], v[230:233], v[200:203], v[42:45]
	v_mfma_f32_16x16x32_bf16 v[38:41], v[238:241], v[200:203], v[38:41]
	v_mfma_f32_16x16x32_bf16 v[30:33], v[230:233], v[208:211], v[30:33]
	v_mfma_f32_16x16x32_bf16 v[26:29], v[238:241], v[208:211], v[26:29]
	s_setprio 0
	s_add_i32 s33, 0, 0x18000
	v_add_u32_e32 v139, s33, v148
	s_barrier
	ds_read_b128 v[156:159], v139
	ds_read_b128 v[160:163], v139 offset:1024
	ds_read_b128 v[172:175], v139 offset:2048
	ds_read_b128 v[176:179], v139 offset:3072
	s_mov_b32 m0, s30
	ds_read_b128 v[180:183], v151 offset:32768
	ds_read_b128 v[184:187], v151 offset:33792
	ds_read_b128 v[188:191], v151 offset:34816
	ds_read_b128 v[192:195], v151 offset:35840
	ds_read_b128 v[196:199], v151 offset:36864
	ds_read_b128 v[200:203], v151 offset:37888
	ds_read_b128 v[204:207], v151 offset:38912
	ds_read_b128 v[208:211], v151 offset:39936
	global_load_lds_dwordx4 v135, s[20:21]
	s_mov_b32 m0, s31
	s_nop 0
	global_load_lds_dwordx4 v137, s[20:21]
	s_waitcnt lgkmcnt(8)
	s_barrier
	s_waitcnt lgkmcnt(0)
	s_setprio 1
	s_waitcnt lgkmcnt(0)
	v_mfma_f32_16x16x32_bf16 v[126:129], v[156:159], v[180:183], v[126:129]
	v_mfma_f32_16x16x32_bf16 v[122:125], v[172:175], v[180:183], v[122:125]
	v_mfma_f32_16x16x32_bf16 v[118:121], v[156:159], v[188:191], v[118:121]
	v_mfma_f32_16x16x32_bf16 v[110:113], v[172:175], v[188:191], v[110:113]
	v_mfma_f32_16x16x32_bf16 v[102:105], v[156:159], v[196:199], v[102:105]
	v_mfma_f32_16x16x32_bf16 v[94:97], v[172:175], v[196:199], v[94:97]
	v_mfma_f32_16x16x32_bf16 v[86:89], v[156:159], v[204:207], v[86:89]
	v_mfma_f32_16x16x32_bf16 v[78:81], v[172:175], v[204:207], v[78:81]
	v_mfma_f32_16x16x32_bf16 v[126:129], v[160:163], v[184:187], v[126:129]
	v_mfma_f32_16x16x32_bf16 v[122:125], v[176:179], v[184:187], v[122:125]
	v_mfma_f32_16x16x32_bf16 v[118:121], v[160:163], v[192:195], v[118:121]
	v_mfma_f32_16x16x32_bf16 v[110:113], v[176:179], v[192:195], v[110:113]
	v_mfma_f32_16x16x32_bf16 v[102:105], v[160:163], v[200:203], v[102:105]
	v_mfma_f32_16x16x32_bf16 v[94:97], v[176:179], v[200:203], v[94:97]
	v_mfma_f32_16x16x32_bf16 v[86:89], v[160:163], v[208:211], v[86:89]
	v_mfma_f32_16x16x32_bf16 v[78:81], v[176:179], v[208:211], v[78:81]
	s_setprio 0
	s_barrier
	s_add_i32 s20, 0, 0x1c000
	s_add_i32 s21, s33, s26
	v_add_u32_e32 v135, s20, v148
	v_lshl_add_u64 v[242:243], v[242:243], 0, s[96:97]
	s_mov_b32 m0, s21
	ds_read_b128 v[212:215], v135
	ds_read_b128 v[230:233], v135 offset:1024
	ds_read_b128 v[234:237], v135 offset:2048
	ds_read_b128 v[238:241], v135 offset:3072
	global_load_lds_dwordx4 v[242:243], off
	v_lshl_add_u64 v[242:243], v[244:245], 0, s[96:97]
	s_add_i32 m0, s21, 0x2000
	s_nop 0
	global_load_lds_dwordx4 v[242:243], off
	s_barrier
	s_waitcnt lgkmcnt(0)
	s_setprio 1
	s_waitcnt lgkmcnt(0)
	v_mfma_f32_16x16x32_bf16 v[114:117], v[212:215], v[180:183], v[114:117]
	v_mfma_f32_16x16x32_bf16 v[106:109], v[234:237], v[180:183], v[106:109]
	v_mfma_f32_16x16x32_bf16 v[98:101], v[212:215], v[188:191], v[98:101]
	v_mfma_f32_16x16x32_bf16 v[90:93], v[234:237], v[188:191], v[90:93]
	v_mfma_f32_16x16x32_bf16 v[82:85], v[212:215], v[196:199], v[82:85]
	v_mfma_f32_16x16x32_bf16 v[74:77], v[234:237], v[196:199], v[74:77]
	v_mfma_f32_16x16x32_bf16 v[62:65], v[212:215], v[204:207], v[62:65]
	v_mfma_f32_16x16x32_bf16 v[58:61], v[234:237], v[204:207], v[58:61]
	v_mfma_f32_16x16x32_bf16 v[114:117], v[230:233], v[184:187], v[114:117]
	v_mfma_f32_16x16x32_bf16 v[106:109], v[238:241], v[184:187], v[106:109]
	v_mfma_f32_16x16x32_bf16 v[98:101], v[230:233], v[192:195], v[98:101]
	v_mfma_f32_16x16x32_bf16 v[90:93], v[238:241], v[192:195], v[90:93]
	v_mfma_f32_16x16x32_bf16 v[82:85], v[230:233], v[200:203], v[82:85]
	v_mfma_f32_16x16x32_bf16 v[74:77], v[238:241], v[200:203], v[74:77]
	v_mfma_f32_16x16x32_bf16 v[62:65], v[230:233], v[208:211], v[62:65]
	v_mfma_f32_16x16x32_bf16 v[58:61], v[238:241], v[208:211], v[58:61]
	s_setprio 0
	s_mov_b32 m0, s34
	v_lshl_add_u64 v[242:243], v[246:247], 0, s[96:97]
	s_barrier
	ds_read_b128 v[180:183], v151 offset:49152
	ds_read_b128 v[184:187], v151 offset:50176
	ds_read_b128 v[188:191], v151 offset:51200
	ds_read_b128 v[192:195], v151 offset:52224
	ds_read_b128 v[196:199], v151 offset:53248
	ds_read_b128 v[200:203], v151 offset:54272
	ds_read_b128 v[204:207], v151 offset:55296
	ds_read_b128 v[208:211], v151 offset:56320
	global_load_lds_dwordx4 v[242:243], off
	v_lshl_add_u64 v[164:165], v[164:165], 0, s[96:97]
	s_mov_b32 m0, s35
	s_nop 0
	global_load_lds_dwordx4 v[164:165], off
	s_barrier
	s_waitcnt lgkmcnt(0)
	s_setprio 1
	s_waitcnt lgkmcnt(0)
	v_mfma_f32_16x16x32_bf16 v[46:49], v[156:159], v[180:183], v[46:49]
	v_mfma_f32_16x16x32_bf16 v[34:37], v[172:175], v[180:183], v[34:37]
	v_mfma_f32_16x16x32_bf16 v[22:25], v[156:159], v[188:191], v[22:25]
	v_mfma_f32_16x16x32_bf16 v[18:21], v[172:175], v[188:191], v[18:21]
	v_mfma_f32_16x16x32_bf16 v[14:17], v[156:159], v[196:199], v[14:17]
	v_mfma_f32_16x16x32_bf16 v[10:13], v[172:175], v[196:199], v[10:13]
	v_mfma_f32_16x16x32_bf16 v[6:9], v[156:159], v[204:207], v[6:9]
	v_mfma_f32_16x16x32_bf16 v[2:5], v[172:175], v[204:207], v[2:5]
	v_mfma_f32_16x16x32_bf16 v[46:49], v[160:163], v[184:187], v[46:49]
	v_mfma_f32_16x16x32_bf16 v[34:37], v[176:179], v[184:187], v[34:37]
	v_mfma_f32_16x16x32_bf16 v[22:25], v[160:163], v[192:195], v[22:25]
	v_mfma_f32_16x16x32_bf16 v[18:21], v[176:179], v[192:195], v[18:21]
	v_mfma_f32_16x16x32_bf16 v[14:17], v[160:163], v[200:203], v[14:17]
	v_mfma_f32_16x16x32_bf16 v[10:13], v[176:179], v[200:203], v[10:13]
	v_mfma_f32_16x16x32_bf16 v[6:9], v[160:163], v[208:211], v[6:9]
	v_mfma_f32_16x16x32_bf16 v[2:5], v[176:179], v[208:211], v[2:5]
	s_setprio 0
	s_barrier
	s_add_u32 s18, s18, 0x40080
	s_addc_u32 s19, s19, 0
	s_add_i32 s20, s20, s26
	v_lshl_add_u64 v[156:157], s[18:19], 0, v[132:133]
	s_mov_b32 m0, s20
	s_nop 0
	global_load_lds_dwordx4 v[156:157], off
	v_lshl_add_u64 v[156:157], s[18:19], 0, v[130:131]
	s_add_i32 m0, s20, 0x2000
	s_nop 0
	global_load_lds_dwordx4 v[156:157], off
	s_waitcnt vmcnt(6)
	s_barrier
	s_setprio 1
	v_mfma_f32_16x16x32_bf16 v[70:73], v[212:215], v[180:183], v[70:73]
	v_mfma_f32_16x16x32_bf16 v[66:69], v[234:237], v[180:183], v[66:69]
	v_mfma_f32_16x16x32_bf16 v[54:57], v[212:215], v[188:191], v[54:57]
	v_mfma_f32_16x16x32_bf16 v[50:53], v[234:237], v[188:191], v[50:53]
	v_mfma_f32_16x16x32_bf16 v[42:45], v[212:215], v[196:199], v[42:45]
	v_mfma_f32_16x16x32_bf16 v[38:41], v[234:237], v[196:199], v[38:41]
	v_mfma_f32_16x16x32_bf16 v[30:33], v[212:215], v[204:207], v[30:33]
	v_mfma_f32_16x16x32_bf16 v[26:29], v[234:237], v[204:207], v[26:29]
	v_mfma_f32_16x16x32_bf16 v[70:73], v[230:233], v[184:187], v[70:73]
	v_mfma_f32_16x16x32_bf16 v[66:69], v[238:241], v[184:187], v[66:69]
	v_mfma_f32_16x16x32_bf16 v[54:57], v[230:233], v[192:195], v[54:57]
	v_mfma_f32_16x16x32_bf16 v[50:53], v[238:241], v[192:195], v[50:53]
	v_mfma_f32_16x16x32_bf16 v[42:45], v[230:233], v[200:203], v[42:45]
	v_mfma_f32_16x16x32_bf16 v[38:41], v[238:241], v[200:203], v[38:41]
	v_mfma_f32_16x16x32_bf16 v[30:33], v[230:233], v[208:211], v[30:33]
	v_mfma_f32_16x16x32_bf16 v[26:29], v[238:241], v[208:211], v[26:29]
	s_setprio 0
	s_add_i32 s44, s44, 2
	s_add_u32 s16, s16, 0x100
	s_addc_u32 s17, s17, 0
	s_cmp_gt_u32 s44, 13
	s_barrier
	s_cbranch_scc0 .LBB0_268
	s_branch .Lgi_epi
.Lgi_half:
	s_cmp_eq_u32 s100, 0
	s_cbranch_scc0 .Lgi_loop1
.Lgi_loop0:
	s_add_u32 s18, s8, s16
	s_addc_u32 s19, s9, s17
	s_add_u32 s20, s18, 0x100
	s_addc_u32 s21, s19, 0
	s_add_u32 s33, s42, s16
	s_addc_u32 s45, s43, s17
	s_cmpk_eq_i32 s16, 0x700
	s_cselect_b64 s[46:47], -1, 0
	s_and_b64 s[18:19], s[46:47], exec
	s_cselect_b32 s21, s9, s21
	s_cselect_b32 s20, s8, s20
	s_cselect_b32 s19, s13, s45
	s_cselect_b32 s18, s41, s33
	s_add_i32 s33, 0, 0x10000
	v_add_u32_e32 v135, s33, v148
	ds_read_b128 v[156:159], v135
	ds_read_b128 v[160:163], v135 offset:1024
	ds_read_b128 v[172:175], v135 offset:2048
	ds_read_b128 v[176:179], v135 offset:3072
	s_and_b64 vcc, s[6:7], s[46:47]
	v_cndmask_b32_e32 v226, v134, v152, vcc
	v_cndmask_b32_e32 v164, v136, v153, vcc
	v_cndmask_b32_e32 v135, v138, v154, vcc
	v_cndmask_b32_e32 v137, v140, v155, vcc
	v_lshl_add_u64 v[212:213], v[144:145], 0, s[16:17]
	s_add_i32 m0, s28, 0xc000
	ds_read_b128 v[180:183], v151
	ds_read_b128 v[184:187], v151 offset:1024
	ds_read_b128 v[188:191], v151 offset:2048
	ds_read_b128 v[192:195], v151 offset:3072
	ds_read_b128 v[196:199], v151 offset:4096
	ds_read_b128 v[200:203], v151 offset:5120
	ds_read_b128 v[204:207], v151 offset:6144
	ds_read_b128 v[208:211], v151 offset:7168
	global_load_lds_dwordx4 v[212:213], off
	v_lshl_add_u64 v[212:213], v[142:143], 0, s[16:17]
	s_add_i32 m0, s28, 0xe000
	s_nop 0
	global_load_lds_dwordx4 v[212:213], off
	s_waitcnt lgkmcnt(8)
	s_barrier
	s_waitcnt lgkmcnt(0)
	s_setprio 1
	s_waitcnt lgkmcnt(0)
	s_setprio 0
	s_barrier
	s_add_i32 s45, 0, 0x14000
	s_add_i32 s33, s33, s26
	v_add_u32_e32 v139, s45, v148
	v_lshl_add_u64 v[242:243], s[18:19], 0, v[132:133]
	s_mov_b32 m0, s33
	ds_read_b128 v[212:215], v139
	ds_read_b128 v[230:233], v139 offset:1024
	ds_read_b128 v[234:237], v139 offset:2048
	ds_read_b128 v[238:241], v139 offset:3072
	global_load_lds_dwordx4 v[242:243], off
	v_lshl_add_u64 v[244:245], s[18:19], 0, v[130:131]
	s_add_i32 m0, s33, 0x2000
	s_nop 0
	global_load_lds_dwordx4 v[244:245], off
	s_barrier
	s_waitcnt lgkmcnt(0)
	s_setprio 1
	s_waitcnt lgkmcnt(0)
	s_setprio 0
	s_mov_b32 m0, s28
	s_barrier
	ds_read_b128 v[180:183], v151 offset:16384
	ds_read_b128 v[184:187], v151 offset:17408
	ds_read_b128 v[188:191], v151 offset:18432
	ds_read_b128 v[192:195], v151 offset:19456
	ds_read_b128 v[196:199], v151 offset:20480
	ds_read_b128 v[200:203], v151 offset:21504
	ds_read_b128 v[204:207], v151 offset:22528
	ds_read_b128 v[208:211], v151 offset:23552
	global_load_lds_dwordx4 v226, s[20:21]
	s_mov_b32 m0, s29
	v_mov_b32_e32 v165, v227
	global_load_lds_dwordx4 v164, s[20:21]
	s_barrier
	s_waitcnt lgkmcnt(0)
	v_lshl_add_u64 v[246:247], s[20:21], 0, v[226:227]
	v_lshl_add_u64 v[164:165], s[20:21], 0, v[164:165]
	s_setprio 1
	s_waitcnt lgkmcnt(0)
	v_mfma_f32_16x16x32_bf16 v[46:49], v[156:159], v[180:183], v[46:49]
	v_mfma_f32_16x16x32_bf16 v[34:37], v[172:175], v[180:183], v[34:37]
	v_mfma_f32_16x16x32_bf16 v[22:25], v[156:159], v[188:191], v[22:25]
	v_mfma_f32_16x16x32_bf16 v[18:21], v[172:175], v[188:191], v[18:21]
	v_mfma_f32_16x16x32_bf16 v[14:17], v[156:159], v[196:199], v[14:17]
	v_mfma_f32_16x16x32_bf16 v[10:13], v[172:175], v[196:199], v[10:13]
	v_mfma_f32_16x16x32_bf16 v[6:9], v[156:159], v[204:207], v[6:9]
	v_mfma_f32_16x16x32_bf16 v[2:5], v[172:175], v[204:207], v[2:5]
	v_mfma_f32_16x16x32_bf16 v[46:49], v[160:163], v[184:187], v[46:49]
	v_mfma_f32_16x16x32_bf16 v[34:37], v[176:179], v[184:187], v[34:37]
	v_mfma_f32_16x16x32_bf16 v[22:25], v[160:163], v[192:195], v[22:25]
	v_mfma_f32_16x16x32_bf16 v[18:21], v[176:179], v[192:195], v[18:21]
	v_mfma_f32_16x16x32_bf16 v[14:17], v[160:163], v[200:203], v[14:17]
	v_mfma_f32_16x16x32_bf16 v[10:13], v[176:179], v[200:203], v[10:13]
	v_mfma_f32_16x16x32_bf16 v[6:9], v[160:163], v[208:211], v[6:9]
	v_mfma_f32_16x16x32_bf16 v[2:5], v[176:179], v[208:211], v[2:5]
	s_setprio 0
	s_barrier
	s_add_u32 s46, s18, 0x40000
	s_addc_u32 s47, s19, 0
	s_add_i32 s33, s45, s26
	v_lshl_add_u64 v[156:157], s[46:47], 0, v[132:133]
	s_mov_b32 m0, s33
	s_nop 0
	global_load_lds_dwordx4 v[156:157], off
	v_lshl_add_u64 v[156:157], s[46:47], 0, v[130:131]
	s_add_i32 m0, s33, 0x2000
	s_nop 0
	global_load_lds_dwordx4 v[156:157], off
	s_waitcnt vmcnt(6)
	s_barrier
	s_setprio 1
	v_mfma_f32_16x16x32_bf16 v[70:73], v[212:215], v[180:183], v[70:73]
	v_mfma_f32_16x16x32_bf16 v[66:69], v[234:237], v[180:183], v[66:69]
	v_mfma_f32_16x16x32_bf16 v[54:57], v[212:215], v[188:191], v[54:57]
	v_mfma_f32_16x16x32_bf16 v[50:53], v[234:237], v[188:191], v[50:53]
	v_mfma_f32_16x16x32_bf16 v[42:45], v[212:215], v[196:199], v[42:45]
	v_mfma_f32_16x16x32_bf16 v[38:41], v[234:237], v[196:199], v[38:41]
	v_mfma_f32_16x16x32_bf16 v[30:33], v[212:215], v[204:207], v[30:33]
	v_mfma_f32_16x16x32_bf16 v[26:29], v[234:237], v[204:207], v[26:29]
	v_mfma_f32_16x16x32_bf16 v[70:73], v[230:233], v[184:187], v[70:73]
	v_mfma_f32_16x16x32_bf16 v[66:69], v[238:241], v[184:187], v[66:69]
	v_mfma_f32_16x16x32_bf16 v[54:57], v[230:233], v[192:195], v[54:57]
	v_mfma_f32_16x16x32_bf16 v[50:53], v[238:241], v[192:195], v[50:53]
	v_mfma_f32_16x16x32_bf16 v[42:45], v[230:233], v[200:203], v[42:45]
	v_mfma_f32_16x16x32_bf16 v[38:41], v[238:241], v[200:203], v[38:41]
	v_mfma_f32_16x16x32_bf16 v[30:33], v[230:233], v[208:211], v[30:33]
	v_mfma_f32_16x16x32_bf16 v[26:29], v[238:241], v[208:211], v[26:29]
	s_setprio 0
	s_add_i32 s33, 0, 0x18000
	v_add_u32_e32 v139, s33, v148
	s_barrier
	ds_read_b128 v[156:159], v139
	ds_read_b128 v[160:163], v139 offset:1024
	ds_read_b128 v[172:175], v139 offset:2048
	ds_read_b128 v[176:179], v139 offset:3072
	s_mov_b32 m0, s30
	ds_read_b128 v[180:183], v151 offset:32768
	ds_read_b128 v[184:187], v151 offset:33792
	ds_read_b128 v[188:191], v151 offset:34816
	ds_read_b128 v[192:195], v151 offset:35840
	ds_read_b128 v[196:199], v151 offset:36864
	ds_read_b128 v[200:203], v151 offset:37888
	ds_read_b128 v[204:207], v151 offset:38912
	ds_read_b128 v[208:211], v151 offset:39936
	global_load_lds_dwordx4 v135, s[20:21]
	s_mov_b32 m0, s31
	s_nop 0
	global_load_lds_dwordx4 v137, s[20:21]
	s_waitcnt lgkmcnt(8)
	s_barrier
	s_waitcnt lgkmcnt(0)
	s_setprio 1
	s_waitcnt lgkmcnt(0)
	s_setprio 0
	s_barrier
	s_add_i32 s20, 0, 0x1c000
	s_add_i32 s21, s33, s26
	v_add_u32_e32 v135, s20, v148
	v_lshl_add_u64 v[242:243], v[242:243], 0, s[96:97]
	s_mov_b32 m0, s21
	ds_read_b128 v[212:215], v135
	ds_read_b128 v[230:233], v135 offset:1024
	ds_read_b128 v[234:237], v135 offset:2048
	ds_read_b128 v[238:241], v135 offset:3072
	global_load_lds_dwordx4 v[242:243], off
	v_lshl_add_u64 v[242:243], v[244:245], 0, s[96:97]
	s_add_i32 m0, s21, 0x2000
	s_nop 0
	global_load_lds_dwordx4 v[242:243], off
	s_barrier
	s_waitcnt lgkmcnt(0)
	s_setprio 1
	s_waitcnt lgkmcnt(0)
	s_setprio 0
	s_mov_b32 m0, s34
	v_lshl_add_u64 v[242:243], v[246:247], 0, s[96:97]
	s_barrier
	ds_read_b128 v[180:183], v151 offset:49152
	ds_read_b128 v[184:187], v151 offset:50176
	ds_read_b128 v[188:191], v151 offset:51200
	ds_read_b128 v[192:195], v151 offset:52224
	ds_read_b128 v[196:199], v151 offset:53248
	ds_read_b128 v[200:203], v151 offset:54272
	ds_read_b128 v[204:207], v151 offset:55296
	ds_read_b128 v[208:211], v151 offset:56320
	global_load_lds_dwordx4 v[242:243], off
	v_lshl_add_u64 v[164:165], v[164:165], 0, s[96:97]
	s_mov_b32 m0, s35
	s_nop 0
	global_load_lds_dwordx4 v[164:165], off
	s_barrier
	s_waitcnt lgkmcnt(0)
	s_setprio 1
	s_waitcnt lgkmcnt(0)
	v_mfma_f32_16x16x32_bf16 v[46:49], v[156:159], v[180:183], v[46:49]
	v_mfma_f32_16x16x32_bf16 v[34:37], v[172:175], v[180:183], v[34:37]
	v_mfma_f32_16x16x32_bf16 v[22:25], v[156:159], v[188:191], v[22:25]
	v_mfma_f32_16x16x32_bf16 v[18:21], v[172:175], v[188:191], v[18:21]
	v_mfma_f32_16x16x32_bf16 v[14:17], v[156:159], v[196:199], v[14:17]
	v_mfma_f32_16x16x32_bf16 v[10:13], v[172:175], v[196:199], v[10:13]
	v_mfma_f32_16x16x32_bf16 v[6:9], v[156:159], v[204:207], v[6:9]
	v_mfma_f32_16x16x32_bf16 v[2:5], v[172:175], v[204:207], v[2:5]
	v_mfma_f32_16x16x32_bf16 v[46:49], v[160:163], v[184:187], v[46:49]
	v_mfma_f32_16x16x32_bf16 v[34:37], v[176:179], v[184:187], v[34:37]
	v_mfma_f32_16x16x32_bf16 v[22:25], v[160:163], v[192:195], v[22:25]
	v_mfma_f32_16x16x32_bf16 v[18:21], v[176:179], v[192:195], v[18:21]
	v_mfma_f32_16x16x32_bf16 v[14:17], v[160:163], v[200:203], v[14:17]
	v_mfma_f32_16x16x32_bf16 v[10:13], v[176:179], v[200:203], v[10:13]
	v_mfma_f32_16x16x32_bf16 v[6:9], v[160:163], v[208:211], v[6:9]
	v_mfma_f32_16x16x32_bf16 v[2:5], v[176:179], v[208:211], v[2:5]
	s_setprio 0
	s_barrier
	s_add_u32 s18, s18, 0x40080
	s_addc_u32 s19, s19, 0
	s_add_i32 s20, s20, s26
	v_lshl_add_u64 v[156:157], s[18:19], 0, v[132:133]
	s_mov_b32 m0, s20
	s_nop 0
	global_load_lds_dwordx4 v[156:157], off
	v_lshl_add_u64 v[156:157], s[18:19], 0, v[130:131]
	s_add_i32 m0, s20, 0x2000
	s_nop 0
	global_load_lds_dwordx4 v[156:157], off
	s_waitcnt vmcnt(6)
	s_barrier
	s_setprio 1
	v_mfma_f32_16x16x32_bf16 v[70:73], v[212:215], v[180:183], v[70:73]
	v_mfma_f32_16x16x32_bf16 v[66:69], v[234:237], v[180:183], v[66:69]
	v_mfma_f32_16x16x32_bf16 v[54:57], v[212:215], v[188:191], v[54:57]
	v_mfma_f32_16x16x32_bf16 v[50:53], v[234:237], v[188:191], v[50:53]
	v_mfma_f32_16x16x32_bf16 v[42:45], v[212:215], v[196:199], v[42:45]
	v_mfma_f32_16x16x32_bf16 v[38:41], v[234:237], v[196:199], v[38:41]
	v_mfma_f32_16x16x32_bf16 v[30:33], v[212:215], v[204:207], v[30:33]
	v_mfma_f32_16x16x32_bf16 v[26:29], v[234:237], v[204:207], v[26:29]
	v_mfma_f32_16x16x32_bf16 v[70:73], v[230:233], v[184:187], v[70:73]
	v_mfma_f32_16x16x32_bf16 v[66:69], v[238:241], v[184:187], v[66:69]
	v_mfma_f32_16x16x32_bf16 v[54:57], v[230:233], v[192:195], v[54:57]
	v_mfma_f32_16x16x32_bf16 v[50:53], v[238:241], v[192:195], v[50:53]
	v_mfma_f32_16x16x32_bf16 v[42:45], v[230:233], v[200:203], v[42:45]
	v_mfma_f32_16x16x32_bf16 v[38:41], v[238:241], v[200:203], v[38:41]
	v_mfma_f32_16x16x32_bf16 v[30:33], v[230:233], v[208:211], v[30:33]
	v_mfma_f32_16x16x32_bf16 v[26:29], v[238:241], v[208:211], v[26:29]
	s_setprio 0
	s_add_i32 s44, s44, 2
	s_add_u32 s16, s16, 0x100
	s_addc_u32 s17, s17, 0
	s_cmp_gt_u32 s44, 13
	s_barrier
	s_cbranch_scc0 .Lgi_loop0
	s_branch .Lgi_epi
.Lgi_loop1:
	s_add_u32 s18, s8, s16
	s_addc_u32 s19, s9, s17
	s_add_u32 s20, s18, 0x100
	s_addc_u32 s21, s19, 0
	s_add_u32 s33, s42, s16
	s_addc_u32 s45, s43, s17
	s_cmpk_eq_i32 s16, 0x700
	s_cselect_b64 s[46:47], -1, 0
	s_and_b64 s[18:19], s[46:47], exec
	s_cselect_b32 s21, s9, s21
	s_cselect_b32 s20, s8, s20
	s_cselect_b32 s19, s13, s45
	s_cselect_b32 s18, s41, s33
	s_add_i32 s33, 0, 0x10000
	v_add_u32_e32 v135, s33, v148
	ds_read_b128 v[156:159], v135
	ds_read_b128 v[160:163], v135 offset:1024
	ds_read_b128 v[172:175], v135 offset:2048
	ds_read_b128 v[176:179], v135 offset:3072
	s_and_b64 vcc, s[6:7], s[46:47]
	v_cndmask_b32_e32 v226, v134, v152, vcc
	v_cndmask_b32_e32 v164, v136, v153, vcc
	v_cndmask_b32_e32 v135, v138, v154, vcc
	v_cndmask_b32_e32 v137, v140, v155, vcc
	v_lshl_add_u64 v[212:213], v[144:145], 0, s[16:17]
	s_add_i32 m0, s28, 0xc000
	ds_read_b128 v[180:183], v151
	ds_read_b128 v[184:187], v151 offset:1024
	ds_read_b128 v[188:191], v151 offset:2048
	ds_read_b128 v[192:195], v151 offset:3072
	ds_read_b128 v[196:199], v151 offset:4096
	ds_read_b128 v[200:203], v151 offset:5120
	ds_read_b128 v[204:207], v151 offset:6144
	ds_read_b128 v[208:211], v151 offset:7168
	global_load_lds_dwordx4 v[212:213], off
	v_lshl_add_u64 v[212:213], v[142:143], 0, s[16:17]
	s_add_i32 m0, s28, 0xe000
	s_nop 0
	global_load_lds_dwordx4 v[212:213], off
	s_waitcnt lgkmcnt(8)
	s_barrier
	s_waitcnt lgkmcnt(0)
	s_setprio 1
	s_waitcnt lgkmcnt(0)
	v_mfma_f32_16x16x32_bf16 v[126:129], v[156:159], v[180:183], v[126:129]
	v_mfma_f32_16x16x32_bf16 v[122:125], v[172:175], v[180:183], v[122:125]
	v_mfma_f32_16x16x32_bf16 v[118:121], v[156:159], v[188:191], v[118:121]
	v_mfma_f32_16x16x32_bf16 v[110:113], v[172:175], v[188:191], v[110:113]
	v_mfma_f32_16x16x32_bf16 v[102:105], v[156:159], v[196:199], v[102:105]
	v_mfma_f32_16x16x32_bf16 v[94:97], v[172:175], v[196:199], v[94:97]
	v_mfma_f32_16x16x32_bf16 v[86:89], v[156:159], v[204:207], v[86:89]
	v_mfma_f32_16x16x32_bf16 v[78:81], v[172:175], v[204:207], v[78:81]
	v_mfma_f32_16x16x32_bf16 v[126:129], v[160:163], v[184:187], v[126:129]
	v_mfma_f32_16x16x32_bf16 v[122:125], v[176:179], v[184:187], v[122:125]
	v_mfma_f32_16x16x32_bf16 v[118:121], v[160:163], v[192:195], v[118:121]
	v_mfma_f32_16x16x32_bf16 v[110:113], v[176:179], v[192:195], v[110:113]
	v_mfma_f32_16x16x32_bf16 v[102:105], v[160:163], v[200:203], v[102:105]
	v_mfma_f32_16x16x32_bf16 v[94:97], v[176:179], v[200:203], v[94:97]
	v_mfma_f32_16x16x32_bf16 v[86:89], v[160:163], v[208:211], v[86:89]
	v_mfma_f32_16x16x32_bf16 v[78:81], v[176:179], v[208:211], v[78:81]
	s_setprio 0
	s_barrier
	s_add_i32 s45, 0, 0x14000
	s_add_i32 s33, s33, s26
	v_add_u32_e32 v139, s45, v148
	v_lshl_add_u64 v[242:243], s[18:19], 0, v[132:133]
	s_mov_b32 m0, s33
	ds_read_b128 v[212:215], v139
	ds_read_b128 v[230:233], v139 offset:1024
	ds_read_b128 v[234:237], v139 offset:2048
	ds_read_b128 v[238:241], v139 offset:3072
	global_load_lds_dwordx4 v[242:243], off
	v_lshl_add_u64 v[244:245], s[18:19], 0, v[130:131]
	s_add_i32 m0, s33, 0x2000
	s_nop 0
	global_load_lds_dwordx4 v[244:245], off
	s_barrier
	s_waitcnt lgkmcnt(0)
	s_setprio 1
	s_waitcnt lgkmcnt(0)
	v_mfma_f32_16x16x32_bf16 v[114:117], v[212:215], v[180:183], v[114:117]
	v_mfma_f32_16x16x32_bf16 v[106:109], v[234:237], v[180:183], v[106:109]
	v_mfma_f32_16x16x32_bf16 v[98:101], v[212:215], v[188:191], v[98:101]
	v_mfma_f32_16x16x32_bf16 v[90:93], v[234:237], v[188:191], v[90:93]
	v_mfma_f32_16x16x32_bf16 v[82:85], v[212:215], v[196:199], v[82:85]
	v_mfma_f32_16x16x32_bf16 v[74:77], v[234:237], v[196:199], v[74:77]
	v_mfma_f32_16x16x32_bf16 v[62:65], v[212:215], v[204:207], v[62:65]
	v_mfma_f32_16x16x32_bf16 v[58:61], v[234:237], v[204:207], v[58:61]
	v_mfma_f32_16x16x32_bf16 v[114:117], v[230:233], v[184:187], v[114:117]
	v_mfma_f32_16x16x32_bf16 v[106:109], v[238:241], v[184:187], v[106:109]
	v_mfma_f32_16x16x32_bf16 v[98:101], v[230:233], v[192:195], v[98:101]
	v_mfma_f32_16x16x32_bf16 v[90:93], v[238:241], v[192:195], v[90:93]
	v_mfma_f32_16x16x32_bf16 v[82:85], v[230:233], v[200:203], v[82:85]
	v_mfma_f32_16x16x32_bf16 v[74:77], v[238:241], v[200:203], v[74:77]
	v_mfma_f32_16x16x32_bf16 v[62:65], v[230:233], v[208:211], v[62:65]
	v_mfma_f32_16x16x32_bf16 v[58:61], v[238:241], v[208:211], v[58:61]
	s_setprio 0
	s_mov_b32 m0, s28
	s_barrier
	ds_read_b128 v[180:183], v151 offset:16384
	ds_read_b128 v[184:187], v151 offset:17408
	ds_read_b128 v[188:191], v151 offset:18432
	ds_read_b128 v[192:195], v151 offset:19456
	ds_read_b128 v[196:199], v151 offset:20480
	ds_read_b128 v[200:203], v151 offset:21504
	ds_read_b128 v[204:207], v151 offset:22528
	ds_read_b128 v[208:211], v151 offset:23552
	global_load_lds_dwordx4 v226, s[20:21]
	s_mov_b32 m0, s29
	v_mov_b32_e32 v165, v227
	global_load_lds_dwordx4 v164, s[20:21]
	s_barrier
	s_waitcnt lgkmcnt(0)
	v_lshl_add_u64 v[246:247], s[20:21], 0, v[226:227]
	v_lshl_add_u64 v[164:165], s[20:21], 0, v[164:165]
	s_setprio 1
	s_waitcnt lgkmcnt(0)
	s_setprio 0
	s_barrier
	s_add_u32 s46, s18, 0x40000
	s_addc_u32 s47, s19, 0
	s_add_i32 s33, s45, s26
	v_lshl_add_u64 v[156:157], s[46:47], 0, v[132:133]
	s_mov_b32 m0, s33
	s_nop 0
	global_load_lds_dwordx4 v[156:157], off
	v_lshl_add_u64 v[156:157], s[46:47], 0, v[130:131]
	s_add_i32 m0, s33, 0x2000
	s_nop 0
	global_load_lds_dwordx4 v[156:157], off
	s_waitcnt vmcnt(6)
	s_barrier
	s_setprio 1
	s_setprio 0
	s_add_i32 s33, 0, 0x18000
	v_add_u32_e32 v139, s33, v148
	s_barrier
	ds_read_b128 v[156:159], v139
	ds_read_b128 v[160:163], v139 offset:1024
	ds_read_b128 v[172:175], v139 offset:2048
	ds_read_b128 v[176:179], v139 offset:3072
	s_mov_b32 m0, s30
	ds_read_b128 v[180:183], v151 offset:32768
	ds_read_b128 v[184:187], v151 offset:33792
	ds_read_b128 v[188:191], v151 offset:34816
	ds_read_b128 v[192:195], v151 offset:35840
	ds_read_b128 v[196:199], v151 offset:36864
	ds_read_b128 v[200:203], v151 offset:37888
	ds_read_b128 v[204:207], v151 offset:38912
	ds_read_b128 v[208:211], v151 offset:39936
	global_load_lds_dwordx4 v135, s[20:21]
	s_mov_b32 m0, s31
	s_nop 0
	global_load_lds_dwordx4 v137, s[20:21]
	s_waitcnt lgkmcnt(8)
	s_barrier
	s_waitcnt lgkmcnt(0)
	s_setprio 1
	s_waitcnt lgkmcnt(0)
	v_mfma_f32_16x16x32_bf16 v[126:129], v[156:159], v[180:183], v[126:129]
	v_mfma_f32_16x16x32_bf16 v[122:125], v[172:175], v[180:183], v[122:125]
	v_mfma_f32_16x16x32_bf16 v[118:121], v[156:159], v[188:191], v[118:121]
	v_mfma_f32_16x16x32_bf16 v[110:113], v[172:175], v[188:191], v[110:113]
	v_mfma_f32_16x16x32_bf16 v[102:105], v[156:159], v[196:199], v[102:105]
	v_mfma_f32_16x16x32_bf16 v[94:97], v[172:175], v[196:199], v[94:97]
	v_mfma_f32_16x16x32_bf16 v[86:89], v[156:159], v[204:207], v[86:89]
	v_mfma_f32_16x16x32_bf16 v[78:81], v[172:175], v[204:207], v[78:81]
	v_mfma_f32_16x16x32_bf16 v[126:129], v[160:163], v[184:187], v[126:129]
	v_mfma_f32_16x16x32_bf16 v[122:125], v[176:179], v[184:187], v[122:125]
	v_mfma_f32_16x16x32_bf16 v[118:121], v[160:163], v[192:195], v[118:121]
	v_mfma_f32_16x16x32_bf16 v[110:113], v[176:179], v[192:195], v[110:113]
	v_mfma_f32_16x16x32_bf16 v[102:105], v[160:163], v[200:203], v[102:105]
	v_mfma_f32_16x16x32_bf16 v[94:97], v[176:179], v[200:203], v[94:97]
	v_mfma_f32_16x16x32_bf16 v[86:89], v[160:163], v[208:211], v[86:89]
	v_mfma_f32_16x16x32_bf16 v[78:81], v[176:179], v[208:211], v[78:81]
	s_setprio 0
	s_barrier
	s_add_i32 s20, 0, 0x1c000
	s_add_i32 s21, s33, s26
	v_add_u32_e32 v135, s20, v148
	v_lshl_add_u64 v[242:243], v[242:243], 0, s[96:97]
	s_mov_b32 m0, s21
	ds_read_b128 v[212:215], v135
	ds_read_b128 v[230:233], v135 offset:1024
	ds_read_b128 v[234:237], v135 offset:2048
	ds_read_b128 v[238:241], v135 offset:3072
	global_load_lds_dwordx4 v[242:243], off
	v_lshl_add_u64 v[242:243], v[244:245], 0, s[96:97]
	s_add_i32 m0, s21, 0x2000
	s_nop 0
	global_load_lds_dwordx4 v[242:243], off
	s_barrier
	s_waitcnt lgkmcnt(0)
	s_setprio 1
	s_waitcnt lgkmcnt(0)
	v_mfma_f32_16x16x32_bf16 v[114:117], v[212:215], v[180:183], v[114:117]
	v_mfma_f32_16x16x32_bf16 v[106:109], v[234:237], v[180:183], v[106:109]
	v_mfma_f32_16x16x32_bf16 v[98:101], v[212:215], v[188:191], v[98:101]
	v_mfma_f32_16x16x32_bf16 v[90:93], v[234:237], v[188:191], v[90:93]
	v_mfma_f32_16x16x32_bf16 v[82:85], v[212:215], v[196:199], v[82:85]
	v_mfma_f32_16x16x32_bf16 v[74:77], v[234:237], v[196:199], v[74:77]
	v_mfma_f32_16x16x32_bf16 v[62:65], v[212:215], v[204:207], v[62:65]
	v_mfma_f32_16x16x32_bf16 v[58:61], v[234:237], v[204:207], v[58:61]
	v_mfma_f32_16x16x32_bf16 v[114:117], v[230:233], v[184:187], v[114:117]
	v_mfma_f32_16x16x32_bf16 v[106:109], v[238:241], v[184:187], v[106:109]
	v_mfma_f32_16x16x32_bf16 v[98:101], v[230:233], v[192:195], v[98:101]
	v_mfma_f32_16x16x32_bf16 v[90:93], v[238:241], v[192:195], v[90:93]
	v_mfma_f32_16x16x32_bf16 v[82:85], v[230:233], v[200:203], v[82:85]
	v_mfma_f32_16x16x32_bf16 v[74:77], v[238:241], v[200:203], v[74:77]
	v_mfma_f32_16x16x32_bf16 v[62:65], v[230:233], v[208:211], v[62:65]
	v_mfma_f32_16x16x32_bf16 v[58:61], v[238:241], v[208:211], v[58:61]
	s_setprio 0
	s_mov_b32 m0, s34
	v_lshl_add_u64 v[242:243], v[246:247], 0, s[96:97]
	s_barrier
	ds_read_b128 v[180:183], v151 offset:49152
	ds_read_b128 v[184:187], v151 offset:50176
	ds_read_b128 v[188:191], v151 offset:51200
	ds_read_b128 v[192:195], v151 offset:52224
	ds_read_b128 v[196:199], v151 offset:53248
	ds_read_b128 v[200:203], v151 offset:54272
	ds_read_b128 v[204:207], v151 offset:55296
	ds_read_b128 v[208:211], v151 offset:56320
	global_load_lds_dwordx4 v[242:243], off
	v_lshl_add_u64 v[164:165], v[164:165], 0, s[96:97]
	s_mov_b32 m0, s35
	s_nop 0
	global_load_lds_dwordx4 v[164:165], off
	s_barrier
	s_waitcnt lgkmcnt(0)
	s_setprio 1
	s_waitcnt lgkmcnt(0)
	s_setprio 0
	s_barrier
	s_add_u32 s18, s18, 0x40080
	s_addc_u32 s19, s19, 0
	s_add_i32 s20, s20, s26
	v_lshl_add_u64 v[156:157], s[18:19], 0, v[132:133]
	s_mov_b32 m0, s20
	s_nop 0
	global_load_lds_dwordx4 v[156:157], off
	v_lshl_add_u64 v[156:157], s[18:19], 0, v[130:131]
	s_add_i32 m0, s20, 0x2000
	s_nop 0
	global_load_lds_dwordx4 v[156:157], off
	s_waitcnt vmcnt(6)
	s_barrier
	s_setprio 1
	s_setprio 0
	s_add_i32 s44, s44, 2
	s_add_u32 s16, s16, 0x100
	s_addc_u32 s17, s17, 0
	s_cmp_gt_u32 s44, 13
	s_barrier
	s_cbranch_scc0 .Lgi_loop1
.Lgi_epi:
	v_lshl_or_b32 v136, s40, 8, v150
	v_lshl_add_u32 v140, s39, 8, v147
	v_ashrrev_i32_e32 v137, 31, v136
	v_mov_b64_e32 v[134:135], s[10:11]
	s_movk_i32 s13, 0x1c00
	v_mad_i64_i32 v[138:139], s[6:7], v140, s13, v[134:135]
	v_lshlrev_b64 v[136:137], 1, v[136:137]
	v_lshl_add_u64 v[138:139], v[138:139], 0, v[136:137]
	v_cvt_pk_bf16_f32 v126, v126, v127
	v_cvt_pk_bf16_f32 v127, v128, v129
	v_cvt_pk_bf16_f32 v128, v122, v123
	v_cvt_pk_bf16_f32 v129, v124, v125
	s_cmp_eq_u32 s100, 0
	s_cbranch_scc1 .Lgi_e_0
	global_store_dwordx4 v[138:139], v[126:129], off
.Lgi_e_0:
	v_cvt_pk_bf16_f32 v114, v114, v115
	v_cvt_pk_bf16_f32 v115, v116, v117
	v_cvt_pk_bf16_f32 v116, v106, v107
	v_or_b32_e32 v106, 16, v140
	v_mad_i64_i32 v[106:107], s[6:7], v106, s13, v[134:135]
	v_cvt_pk_bf16_f32 v117, v108, v109
	s_cmp_eq_u32 s100, 0
	s_cbranch_scc1 .Lgi_e_1
	global_store_dwordx4 v[138:139], v[114:117], off offset:256
.Lgi_e_1:
	s_and_b64 vcc, exec, s[4:5]
	v_mov_b32_e32 v138, v154
	v_lshl_add_u64 v[114:115], v[106:107], 0, v[136:137]
	v_cvt_pk_bf16_f32 v106, v118, v119
	v_cvt_pk_bf16_f32 v107, v120, v121
	v_cvt_pk_bf16_f32 v108, v110, v111
	v_cvt_pk_bf16_f32 v109, v112, v113
	s_cmp_eq_u32 s100, 0
	s_cbranch_scc1 .Lgi_e_2
	global_store_dwordx4 v[114:115], v[106:109], off
.Lgi_e_2:
	v_cvt_pk_bf16_f32 v98, v98, v99
	v_cvt_pk_bf16_f32 v99, v100, v101
	v_cvt_pk_bf16_f32 v100, v90, v91
	v_or_b32_e32 v90, 32, v140
	v_mad_i64_i32 v[90:91], s[6:7], v90, s13, v[134:135]
	v_cvt_pk_bf16_f32 v101, v92, v93
	s_cmp_eq_u32 s100, 0
	s_cbranch_scc1 .Lgi_e_3
	global_store_dwordx4 v[114:115], v[98:101], off offset:256
.Lgi_e_3:
	s_mov_b32 s40, s12
	s_mov_b32 s39, s38
	v_lshl_add_u64 v[98:99], v[90:91], 0, v[136:137]
	v_cvt_pk_bf16_f32 v90, v102, v103
	v_cvt_pk_bf16_f32 v91, v104, v105
	v_cvt_pk_bf16_f32 v92, v94, v95
	v_cvt_pk_bf16_f32 v93, v96, v97
	s_cmp_eq_u32 s100, 0
	s_cbranch_scc1 .Lgi_e_4
	global_store_dwordx4 v[98:99], v[90:93], off
.Lgi_e_4:
	v_cvt_pk_bf16_f32 v82, v82, v83
	v_cvt_pk_bf16_f32 v83, v84, v85
	v_cvt_pk_bf16_f32 v84, v74, v75
	v_or_b32_e32 v74, 48, v140
	v_mad_i64_i32 v[74:75], s[6:7], v74, s13, v[134:135]
	v_cvt_pk_bf16_f32 v85, v76, v77
	s_cmp_eq_u32 s100, 0
	s_cbranch_scc1 .Lgi_e_5
	global_store_dwordx4 v[98:99], v[82:85], off offset:256
.Lgi_e_5:
	s_mov_b64 s[16:17], s[14:15]
	s_nop 0
	v_lshl_add_u64 v[82:83], v[74:75], 0, v[136:137]
	v_cvt_pk_bf16_f32 v74, v86, v87
	v_cvt_pk_bf16_f32 v75, v88, v89
	v_cvt_pk_bf16_f32 v76, v78, v79
	v_cvt_pk_bf16_f32 v77, v80, v81
	s_cmp_eq_u32 s100, 0
	s_cbranch_scc1 .Lgi_e_6
	global_store_dwordx4 v[82:83], v[74:77], off
.Lgi_e_6:
	v_cvt_pk_bf16_f32 v62, v62, v63
	v_cvt_pk_bf16_f32 v63, v64, v65
	v_cvt_pk_bf16_f32 v64, v58, v59
	v_add_u32_e32 v58, 0x80, v140
	v_mad_i64_i32 v[58:59], s[6:7], v58, s13, v[134:135]
	v_lshl_add_u64 v[58:59], v[58:59], 0, v[136:137]
	v_cvt_pk_bf16_f32 v65, v60, v61
	s_cmp_eq_u32 s100, 0
	s_cbranch_scc1 .Lgi_e_7
	global_store_dwordx4 v[82:83], v[62:65], off offset:256
.Lgi_e_7:
	v_cvt_pk_bf16_f32 v46, v46, v47
	v_cvt_pk_bf16_f32 v47, v48, v49
	v_cvt_pk_bf16_f32 v48, v34, v35
	v_cvt_pk_bf16_f32 v49, v36, v37
	s_cmp_eq_u32 s100, 1
	s_cbranch_scc1 .Lgi_e_8
	global_store_dwordx4 v[58:59], v[46:49], off
.Lgi_e_8:
	v_cvt_pk_bf16_f32 v34, v70, v71
	v_cvt_pk_bf16_f32 v35, v72, v73
	v_cvt_pk_bf16_f32 v36, v66, v67
	v_cvt_pk_bf16_f32 v37, v68, v69
	s_cmp_eq_u32 s100, 1
	s_cbranch_scc1 .Lgi_e_9
	global_store_dwordx4 v[58:59], v[34:37], off offset:256
.Lgi_e_9:
	v_cvt_pk_bf16_f32 v22, v22, v23
	v_cvt_pk_bf16_f32 v23, v24, v25
	v_cvt_pk_bf16_f32 v24, v18, v19
	v_cvt_pk_bf16_f32 v25, v20, v21
	s_nop 1
	v_add_u32_e32 v34, 0x90, v140
	v_mad_i64_i32 v[34:35], s[6:7], v34, s13, v[134:135]
	v_lshl_add_u64 v[34:35], v[34:35], 0, v[136:137]
	s_cmp_eq_u32 s100, 1
	s_cbranch_scc1 .Lgi_e_10
	global_store_dwordx4 v[34:35], v[22:25], off
.Lgi_e_10:
	v_cvt_pk_bf16_f32 v18, v54, v55
	v_cvt_pk_bf16_f32 v19, v56, v57
	v_cvt_pk_bf16_f32 v20, v50, v51
	v_cvt_pk_bf16_f32 v21, v52, v53
	s_cmp_eq_u32 s100, 1
	s_cbranch_scc1 .Lgi_e_11
	global_store_dwordx4 v[34:35], v[18:21], off offset:256
.Lgi_e_11:
	v_cvt_pk_bf16_f32 v14, v14, v15
	v_cvt_pk_bf16_f32 v15, v16, v17
	v_cvt_pk_bf16_f32 v16, v10, v11
	v_cvt_pk_bf16_f32 v17, v12, v13
	s_nop 1
	v_add_u32_e32 v18, 0xa0, v140
	v_mad_i64_i32 v[18:19], s[6:7], v18, s13, v[134:135]
	v_lshl_add_u64 v[18:19], v[18:19], 0, v[136:137]
	s_cmp_eq_u32 s100, 1
	s_cbranch_scc1 .Lgi_e_12
	global_store_dwordx4 v[18:19], v[14:17], off
.Lgi_e_12:
	v_cvt_pk_bf16_f32 v10, v42, v43
	v_cvt_pk_bf16_f32 v11, v44, v45
	v_cvt_pk_bf16_f32 v12, v38, v39
	v_cvt_pk_bf16_f32 v13, v40, v41
	s_cmp_eq_u32 s100, 1
	s_cbranch_scc1 .Lgi_e_13
	global_store_dwordx4 v[18:19], v[10:13], off offset:256
.Lgi_e_13:
	v_cvt_pk_bf16_f32 v6, v6, v7
	v_cvt_pk_bf16_f32 v7, v8, v9
	v_cvt_pk_bf16_f32 v8, v2, v3
	v_cvt_pk_bf16_f32 v9, v4, v5
	s_nop 1
	v_add_u32_e32 v10, 0xb0, v140
	v_mad_i64_i32 v[10:11], s[6:7], v10, s13, v[134:135]
	v_lshl_add_u64 v[10:11], v[10:11], 0, v[136:137]
	v_mov_b32_e32 v140, v155
	v_mov_b32_e32 v136, v153
	v_mov_b32_e32 v134, v152
	s_cmp_eq_u32 s100, 1
	s_cbranch_scc1 .Lgi_e_14
	global_store_dwordx4 v[10:11], v[6:9], off
.Lgi_e_14:
	v_cvt_pk_bf16_f32 v2, v30, v31
	v_cvt_pk_bf16_f32 v3, v32, v33
	v_cvt_pk_bf16_f32 v4, v26, v27
	v_cvt_pk_bf16_f32 v5, v28, v29
	s_cmp_eq_u32 s100, 1
	s_cbranch_scc1 .Lgi_e_15
	global_store_dwordx4 v[10:11], v[2:5], off offset:256
.Lgi_e_15:
	s_cbranch_vccz .LBB0_265
	s_waitcnt vmcnt(0)
	s_cmpk_gt_u32 s23, 0xff
	s_cbranch_scc1 .LBB0_272
	s_barrier

	.amdhsa_kernel _Z4mega6Params
		.amdhsa_group_segment_fixed_size 0
		.amdhsa_private_segment_fixed_size 0
		.amdhsa_kernarg_size 888
		.amdhsa_user_sgpr_count 2
		.amdhsa_user_sgpr_dispatch_ptr 0
		.amdhsa_user_sgpr_queue_ptr 0
		.amdhsa_user_sgpr_kernarg_segment_ptr 1
		.amdhsa_user_sgpr_dispatch_id 0
		.amdhsa_user_sgpr_kernarg_preload_length 0
		.amdhsa_user_sgpr_kernarg_preload_offset 0
		.amdhsa_user_sgpr_private_segment_size 0
		.amdhsa_uses_dynamic_stack 0
		.amdhsa_enable_private_segment 0
		.amdhsa_system_sgpr_workgroup_id_x 1
		.amdhsa_system_sgpr_workgroup_id_y 0
		.amdhsa_system_sgpr_workgroup_id_z 0
		.amdhsa_system_sgpr_workgroup_info 0
		.amdhsa_system_vgpr_workitem_id 0
		.amdhsa_next_free_vgpr 256
		.amdhsa_next_free_sgpr 102
		.amdhsa_accum_offset 256
		.amdhsa_reserve_vcc 1
		.amdhsa_float_round_mode_32 0
		.amdhsa_float_round_mode_16_64 0
		.amdhsa_float_denorm_mode_32 3
		.amdhsa_float_denorm_mode_16_64 3
		.amdhsa_dx10_clamp 1
		.amdhsa_ieee_mode 1
		.amdhsa_fp16_overflow 0
		.amdhsa_tg_split 0
		.amdhsa_exception_fp_ieee_invalid_op 0
		.amdhsa_exception_fp_denorm_src 0
		.amdhsa_exception_fp_ieee_div_zero 0
		.amdhsa_exception_fp_ieee_overflow 0
		.amdhsa_exception_fp_ieee_underflow 0
		.amdhsa_exception_fp_ieee_inexact 0
		.amdhsa_exception_int_div_zero 0
	.end_amdhsa_kernel

amdhsa.kernels:
  - .agpr_count:     0
    .args:
      - .offset:         0
        .size:           632
        .value_kind:     by_value
      - .offset:         632
        .size:           4
        .value_kind:     hidden_block_count_x
      - .offset:         636
        .size:           4
        .value_kind:     hidden_block_count_y
      - .offset:         640
        .size:           4
        .value_kind:     hidden_block_count_z
      - .offset:         644
        .size:           2
        .value_kind:     hidden_group_size_x
      - .offset:         646
        .size:           2
        .value_kind:     hidden_group_size_y
      - .offset:         648
        .size:           2
        .value_kind:     hidden_group_size_z
      - .offset:         650
        .size:           2
        .value_kind:     hidden_remainder_x
      - .offset:         652
        .size:           2
        .value_kind:     hidden_remainder_y
      - .offset:         654
        .size:           2
        .value_kind:     hidden_remainder_z
      - .offset:         672
        .size:           8
        .value_kind:     hidden_global_offset_x
      - .offset:         680
        .size:           8
        .value_kind:     hidden_global_offset_y
      - .offset:         688
        .size:           8
        .value_kind:     hidden_global_offset_z
      - .offset:         696
        .size:           2
        .value_kind:     hidden_grid_dims
      - .offset:         752
        .size:           4
        .value_kind:     hidden_dynamic_lds_size
    .group_segment_fixed_size: 0
    .kernarg_segment_align: 8
    .kernarg_segment_size: 888
    .language:       OpenCL C
    .language_version:
      - 2
      - 0
    .max_flat_workgroup_size: 512
    .name:           _Z4mega6Params
    .private_segment_fixed_size: 0
    .sgpr_count:     108
    .sgpr_spill_count: 48
    .symbol:         _Z4mega6Params.kd
    .uniform_work_group_size: 1
    .uses_dynamic_stack: false
    .vgpr_count:     256
    .vgpr_spill_count: 0
    .wavefront_size: 64
